# v41 + rope_conv phase: q/k pieces of RoPE passes 2 and 3 loaded behind pass 1's loads, cos/sin entries kept in registers (no re-load behind each pass's stores)
# baseline (speedup 1.0000x reference)
; #define GAS __attribute__((address_space(1)))
; __device__ __forceinline__ unsigned pk2(float lo, float hi) { return pg8::cvt_pk_bf16(lo, hi); }
; __device__ __forceinline__ void rope_conv_phase(Frame& F) {
;     ...
; #pragma unroll
;             for (int ps = 0; ps < 3; ++ps) { const int li = ps * 64 + F.lane;
;                 if (li < 160) { const int hd = li >> 4, sub = li & 15, half = sub >> 3, d4 = (sub & 7) * 4;
;                     const int col = (hd < 8 ? hd * 128 : 1024 + (hd - 8) * 128) + half * 64 + d4;
;                     const int pos = half ? 128 + (t & 63) : (t >> 6);
;                     const f32x4 cs = *(const GAS f32x4*)(rope + pos * 32 + d4), sn = *(const GAS f32x4*)(rope + 192 * 32 + pos * 32 + d4);
;                     const v2u a = *(const GAS v2u*)(zr + col), b = *(const GAS v2u*)(zr + col + 32);
;                     const float x0 = bflo(a.x), x1 = bfhi(a.x), x2 = bflo(a.y), x3 = bfhi(a.y), y0 = bflo(b.x), y1 = bfhi(b.x), y2 = bflo(b.y), y3 = bfhi(b.y);
;                     v2u oa, ob; oa.x = pk2(x0 * cs.x - y0 * sn.x, x1 * cs.y - y1 * sn.y); oa.y = pk2(x2 * cs.z - y2 * sn.z, x3 * cs.w - y3 * sn.w);
;                     ob.x = pk2(y0 * cs.x + x0 * sn.x, y1 * cs.y + x1 * sn.y); ob.y = pk2(y2 * cs.z + x2 * sn.z, y3 * cs.w + x3 * sn.w);
;                     *(GAS v2u*)(zr + col) = oa; *(GAS v2u*)(zr + col + 32) = ob; } }
.LBB0_352:
	s_cmpk_gt_i32 s13, 0x3fff
	s_movk_i32 s20, 0xff
	s_cbranch_scc1 .LBB0_356
	s_and_b32 s4, s13, 63
	v_lshl_add_u64 v[2:3], s[88:89], 0, v[56:57]
	s_bitset1_b32 s4, 7
	v_add_co_u32_e32 v16, vcc, 0x26700000, v2
	s_bfe_u32 s5, s13, 0x70006
	s_nop 0
	v_addc_co_u32_e32 v17, vcc, 0, v3, vcc
	v_mov_b32_e32 v2, s4
	v_mov_b32_e32 v3, s5
	v_cndmask_b32_e64 v2, v2, v3, s[0:1]
	v_lshlrev_b32_e32 v32, 7, v2
	v_lshl_add_u64 v[2:3], v[34:35], 0, v[32:33]
	global_load_dwordx2 v[18:19], v[16:17], off
	global_load_dwordx2 v[20:21], v[16:17], off offset:64
	v_lshl_add_u64 v[4:5], v[36:37], 0, v[32:33]
	global_load_dwordx4 v[8:11], v[2:3], off
	global_load_dwordx4 v[12:15], v[4:5], off
	s_mov_b32 s100, 0x26700000
	s_mov_b32 s101, 0
	v_lshl_add_u64 v[136:137], s[88:89], 0, v[58:59]
	v_lshl_add_u64 v[136:137], v[136:137], 0, s[100:101]
	global_load_dwordx2 v[120:121], v[136:137], off offset:1088
	global_load_dwordx2 v[122:123], v[136:137], off offset:1024
	global_load_dwordx2 v[124:125], v[136:137], off offset:2112
	global_load_dwordx2 v[126:127], v[136:137], off offset:2048
	v_lshl_add_u64 v[6:7], s[88:89], 0, v[58:59]
	v_add_co_u32_e32 v22, vcc, s11, v6
	s_waitcnt vmcnt(7)
	v_lshlrev_b32_e32 v24, 16, v18
	s_waitcnt vmcnt(6)
	v_lshlrev_b32_e32 v25, 16, v20
	v_and_b32_e32 v27, 0xffff0000, v20
	v_and_b32_e32 v26, 0xffff0000, v18
	v_lshlrev_b32_e32 v29, 16, v21
	v_lshlrev_b32_e32 v28, 16, v19
	v_and_b32_e32 v20, 0xffff0000, v19
	s_waitcnt vmcnt(5)
	v_mov_b32_e32 v18, v8
	s_waitcnt vmcnt(4)
	v_mov_b32_e32 v128, v8
	v_mov_b32_e32 v129, v9
	v_mov_b32_e32 v130, v10
	v_mov_b32_e32 v131, v11
	v_mov_b32_e32 v132, v12
	v_mov_b32_e32 v133, v13
	v_mov_b32_e32 v134, v14
	v_mov_b32_e32 v135, v15
	v_mov_b32_e32 v19, v12
	v_mov_b32_e32 v30, v12
	v_mov_b32_e32 v31, v8
	v_mov_b32_e32 v12, v9
	v_mov_b32_e32 v8, v13
	v_mov_b32_e32 v60, v10
	v_mov_b32_e32 v61, v14
	v_and_b32_e32 v21, 0xffff0000, v21
	v_mov_b32_e32 v64, v14
	v_mov_b32_e32 v65, v10
	v_mov_b32_e32 v14, v11
	v_mov_b32_e32 v10, v15
	v_pk_mul_f32 v[12:13], v[12:13], v[26:27]
	v_pk_mul_f32 v[8:9], v[8:9], v[26:27]
	v_pk_mul_f32 v[26:27], v[60:61], v[28:29]
	v_pk_mul_f32 v[18:19], v[18:19], v[24:25]
	v_pk_mul_f32 v[14:15], v[14:15], v[20:21]
	v_pk_mul_f32 v[10:11], v[10:11], v[20:21]
	v_sub_f32_e32 v12, v12, v13
	v_add_f32_e32 v13, v8, v9
	v_sub_f32_e32 v9, v26, v27
	v_pk_mul_f32 v[24:25], v[30:31], v[24:25]
	v_pk_mul_f32 v[28:29], v[64:65], v[28:29]
	v_sub_f32_e32 v18, v18, v19
	v_sub_f32_e32 v14, v14, v15
	v_add_f32_e32 v11, v10, v11
	v_cvt_pk_bf16_f32 v8, v18, v12
	v_cvt_pk_bf16_f32 v9, v9, v14
	v_addc_co_u32_e32 v23, vcc, 0, v7, vcc
	v_add_f32_e32 v19, v24, v25
	v_add_f32_e32 v20, v28, v29
	v_cvt_pk_bf16_f32 v10, v19, v13
	v_cvt_pk_bf16_f32 v11, v20, v11
	global_store_dwordx2 v[16:17], v[8:9], off
	global_store_dwordx2 v[16:17], v[10:11], off offset:64
	s_waitcnt vmcnt(4)
	v_mov_b32_e32 v16, v120
	v_mov_b32_e32 v17, v121
	s_nop 0
	v_mov_b32_e32 v18, v122
	v_mov_b32_e32 v19, v123
	v_mov_b32_e32 v8, v128
	v_mov_b32_e32 v9, v129
	v_mov_b32_e32 v10, v130
	v_mov_b32_e32 v11, v131
	v_mov_b32_e32 v12, v132
	v_mov_b32_e32 v13, v133
	v_mov_b32_e32 v14, v134
	v_mov_b32_e32 v15, v135
	v_lshlrev_b32_e32 v21, 16, v16
	v_lshlrev_b32_e32 v20, 16, v18
	v_mov_b32_e32 v24, v8
	v_mov_b32_e32 v25, v12
	v_mov_b32_e32 v26, v12
	v_mov_b32_e32 v27, v8
	v_and_b32_e32 v29, 0xffff0000, v16
	v_and_b32_e32 v28, 0xffff0000, v18
	v_mov_b32_e32 v12, v9
	v_mov_b32_e32 v8, v13
	v_lshlrev_b32_e32 v31, 16, v17
	v_lshlrev_b32_e32 v30, 16, v19
	v_mov_b32_e32 v60, v10
	v_mov_b32_e32 v61, v14
	v_mov_b32_e32 v64, v14
	v_mov_b32_e32 v65, v10
	v_and_b32_e32 v17, 0xffff0000, v17
	v_and_b32_e32 v16, 0xffff0000, v19
	v_mov_b32_e32 v14, v11
	v_mov_b32_e32 v10, v15
	v_pk_mul_f32 v[18:19], v[24:25], v[20:21]
	v_pk_mul_f32 v[12:13], v[12:13], v[28:29]
	v_pk_mul_f32 v[8:9], v[8:9], v[28:29]
	v_pk_mul_f32 v[24:25], v[60:61], v[30:31]
	v_pk_mul_f32 v[14:15], v[14:15], v[16:17]
	v_pk_mul_f32 v[10:11], v[10:11], v[16:17]
	v_sub_f32_e32 v12, v12, v13
	v_add_f32_e32 v13, v8, v9
	v_sub_f32_e32 v9, v24, v25
	v_pk_mul_f32 v[20:21], v[26:27], v[20:21]
	v_pk_mul_f32 v[26:27], v[64:65], v[30:31]
	v_sub_f32_e32 v16, v18, v19
	v_sub_f32_e32 v14, v14, v15
	v_add_f32_e32 v11, v10, v11
	v_cvt_pk_bf16_f32 v8, v16, v12
	v_cvt_pk_bf16_f32 v9, v9, v14
	v_add_f32_e32 v17, v20, v21
	v_add_f32_e32 v18, v26, v27
	v_cvt_pk_bf16_f32 v10, v17, v13
	v_cvt_pk_bf16_f32 v11, v18, v11
	global_store_dwordx2 v[22:23], v[8:9], off offset:1024
	global_store_dwordx2 v[22:23], v[10:11], off offset:1088
	s_and_saveexec_b64 s[4:5], s[2:3]
	s_cbranch_execz .LBB0_355
	v_add_co_u32_e32 v6, vcc, 0x26700000, v6
	s_waitcnt vmcnt(4)
	v_mov_b32_e32 v8, v128
	v_mov_b32_e32 v9, v129
	v_mov_b32_e32 v10, v130
	v_mov_b32_e32 v11, v131
	s_nop 0
	v_mov_b32_e32 v2, v132
	v_mov_b32_e32 v3, v133
	v_mov_b32_e32 v4, v134
	v_mov_b32_e32 v5, v135
	v_addc_co_u32_e32 v7, vcc, 0, v7, vcc
	v_mov_b32_e32 v12, v124
	v_mov_b32_e32 v13, v125
	v_mov_b32_e32 v14, v126
	v_mov_b32_e32 v15, v127
	v_mov_b32_e32 v16, v8
	v_mov_b32_e32 v17, v2
	v_mov_b32_e32 v18, v2
	v_mov_b32_e32 v19, v8
	v_mov_b32_e32 v2, v9
	v_mov_b32_e32 v20, v10
	v_mov_b32_e32 v21, v4
	v_lshlrev_b32_e32 v25, 16, v12
	v_lshlrev_b32_e32 v24, 16, v14
	v_and_b32_e32 v27, 0xffff0000, v12
	v_and_b32_e32 v26, 0xffff0000, v14
	v_lshlrev_b32_e32 v29, 16, v13
	v_lshlrev_b32_e32 v28, 16, v15
	v_mov_b32_e32 v8, v3
	v_mov_b32_e32 v22, v4
	v_mov_b32_e32 v23, v10
	v_mov_b32_e32 v4, v11
	v_mov_b32_e32 v10, v5
	v_and_b32_e32 v13, 0xffff0000, v13
	v_and_b32_e32 v12, 0xffff0000, v15
	v_pk_mul_f32 v[14:15], v[16:17], v[24:25]
	v_pk_mul_f32 v[16:17], v[18:19], v[24:25]
	v_pk_mul_f32 v[2:3], v[2:3], v[26:27]
	v_pk_mul_f32 v[18:19], v[20:21], v[28:29]
	v_pk_mul_f32 v[4:5], v[4:5], v[12:13]
	v_pk_mul_f32 v[10:11], v[10:11], v[12:13]
	v_sub_f32_e32 v2, v2, v3
	v_sub_f32_e32 v3, v18, v19
	v_pk_mul_f32 v[8:9], v[8:9], v[26:27]
	v_pk_mul_f32 v[20:21], v[22:23], v[28:29]
	v_sub_f32_e32 v12, v14, v15
	v_sub_f32_e32 v4, v4, v5
	v_add_f32_e32 v5, v10, v11
	v_cvt_pk_bf16_f32 v2, v12, v2
	v_cvt_pk_bf16_f32 v3, v3, v4
	v_add_f32_e32 v13, v16, v17
	v_add_f32_e32 v8, v8, v9
	v_add_f32_e32 v9, v20, v21
	v_cvt_pk_bf16_f32 v4, v13, v8
	v_cvt_pk_bf16_f32 v5, v9, v5
	global_store_dwordx2 v[6:7], v[2:3], off offset:2048
	global_store_dwordx2 v[6:7], v[4:5], off offset:2112
